# de-serialised dependent-load chains: P13 expert-count loads issued together, P2 fgate bias preloaded, P15 slot/gate/x-row loads hoisted and pipelined one iteration ahead
# baseline (speedup 1.0000x reference)
; __device__ __forceinline__ void fgate_groups(Frame& F, const bf16* XN, const bf16* WFT, const float* b_f, float* LOGFT) {
;     ...
;         if (kh == 0) {
;             acc += red[(F.wave >> 1) * 64 + lane];
;             const int row = row0 + fr, b = row / S, s = row % S;
; #pragma unroll
;             for (int r = 0; r < 4; ++r) { const int hh = 4 * fq + r; const float z = acc[r] + b_f[hh];
;                 const float ls = fminf(z, 0.f) - log1pf(__expf(-fabsf(z)));
;                 LOGFT[(size_t)(b * NH + hh) * S + s] = ls * LOG2E; }
.LBB0_224:
	s_and_b64 vcc, exec, s[8:9]
	s_waitcnt lgkmcnt(0)
	s_barrier
	s_cbranch_vccnz .LBB0_219
	global_load_dword v30, v[10:11], off
	global_load_dword v44, v[10:11], off offset:4
	global_load_dword v45, v[10:11], off offset:8
	global_load_dword v46, v[10:11], off offset:12
	ds_read_b128 v[4:7], v12
	s_add_i32 s6, s10, s96
	s_lshl_b32 s6, s6, 3
	v_and_or_b32 v18, s6, -16, v20
	v_ashrrev_i32_e32 v19, 31, v18
	s_waitcnt lgkmcnt(0)
	v_add_f32_e32 v4, v0, v4
	v_lshrrev_b32_e32 v19, 20, v19
	v_add_u32_e32 v19, v18, v19
	v_ashrrev_i32_e32 v0, 12, v19
	v_mul_i32_i24_e32 v19, 0x1000, v0
	v_lshlrev_b32_e32 v0, 4, v0
	v_sub_u32_e32 v18, v18, v19
	v_add_u32_e32 v28, v0, v8
	v_ashrrev_i32_e32 v19, 31, v18
	v_ashrrev_i32_e32 v29, 31, v28
	v_lshl_add_u64 v[18:19], v[18:19], 2, s[86:87]
	v_lshlrev_b64 v[28:29], 14, v[28:29]
	v_lshl_add_u64 v[28:29], v[18:19], 0, v[28:29]
	v_add_f32_e32 v1, v1, v5
	v_add_f32_e32 v2, v2, v6
	s_waitcnt vmcnt(0)
	v_add_f32_e32 v4, v30, v4
	v_mul_f32_e64 v30, |v4|, s13
	v_exp_f32_e32 v32, v30
	v_min_f32_e32 v4, 0, v4
	v_add_f32_e32 v33, 1.0, v32
	v_add_f32_e32 v34, -1.0, v33
	v_frexp_mant_f32_e32 v35, v33
	v_cvt_f64_f32_e32 v[30:31], v33
	v_sub_f32_e32 v36, v34, v33
	v_frexp_exp_i32_f64_e32 v30, v[30:31]
	v_cmp_gt_f32_e32 vcc, s14, v35
	v_sub_f32_e32 v34, v32, v34
	v_add_f32_e32 v31, 1.0, v36
	v_subbrev_co_u32_e32 v30, vcc, 0, v30, vcc
	v_add_f32_e32 v31, v34, v31
	v_sub_u32_e32 v34, 0, v30
	v_cvt_f32_i32_e32 v30, v30
	v_ldexp_f32 v33, v33, v34
	v_ldexp_f32 v31, v31, v34
	v_add_f32_e32 v34, -1.0, v33
	v_add_f32_e32 v35, 1.0, v33
	v_add_f32_e32 v36, 1.0, v34
	v_add_f32_e32 v37, -1.0, v35
	v_sub_f32_e32 v36, v33, v36
	v_sub_f32_e32 v33, v33, v37
	v_mul_f32_e32 v37, 0x3f317218, v30
	v_add_f32_e32 v36, v31, v36
	v_add_f32_e32 v31, v31, v33
	v_fma_f32 v33, v30, s15, -v37
	v_add_f32_e32 v38, v34, v36
	v_add_f32_e32 v39, v35, v31
	v_fmac_f32_e32 v33, 0xb102e308, v30
	v_sub_f32_e32 v30, v38, v34
	v_sub_f32_e32 v34, v39, v35
	v_rcp_f32_e32 v35, v39
	v_add_f32_e32 v40, v37, v33
	v_sub_f32_e32 v31, v31, v34
	v_sub_f32_e32 v34, v40, v37
	v_sub_f32_e32 v33, v33, v34
	v_mul_f32_e32 v34, v38, v35
	v_sub_f32_e32 v30, v36, v30
	v_mul_f32_e32 v36, v39, v34
	v_fma_f32 v37, v34, v39, -v36
	v_fmac_f32_e32 v37, v34, v31
	v_add_f32_e32 v41, v36, v37
	v_sub_f32_e32 v42, v38, v41
	v_sub_f32_e32 v36, v41, v36
	v_sub_f32_e32 v38, v38, v42
	v_sub_f32_e32 v36, v36, v37
	v_sub_f32_e32 v37, v38, v41
	v_add_f32_e32 v30, v30, v37
	v_add_f32_e32 v30, v36, v30
	v_add_f32_e32 v36, v42, v30
	v_mul_f32_e32 v37, v35, v36
	v_sub_f32_e32 v38, v42, v36
	v_mul_f32_e32 v41, v39, v37
	v_add_f32_e32 v30, v30, v38
	v_add_f32_e32 v38, v34, v37
	v_fma_f32 v39, v37, v39, -v41
	v_sub_f32_e32 v34, v38, v34
	v_fmac_f32_e32 v39, v37, v31
	v_sub_f32_e32 v31, v37, v34
	v_add_f32_e32 v34, v41, v39
	v_sub_f32_e32 v37, v34, v41
	v_sub_f32_e32 v41, v36, v34
	v_sub_f32_e32 v36, v36, v41
	v_sub_f32_e32 v34, v36, v34
	v_sub_f32_e32 v37, v37, v39
	v_add_f32_e32 v30, v30, v34
	v_add_f32_e32 v30, v37, v30
	v_add_f32_e32 v30, v41, v30
	v_mul_f32_e32 v30, v35, v30
	v_add_f32_e32 v30, v31, v30
	v_add_f32_e32 v31, v38, v30
	v_mul_f32_e32 v34, v31, v31
	v_fmamk_f32 v37, v34, 0x3e9b6dac, v24
	v_sub_f32_e32 v35, v31, v38
	v_ldexp_f32 v36, v31, 1
	v_mul_f32_e32 v31, v31, v34
	v_fmaak_f32 v34, v34, v37, 0x3f2aaada
	v_mul_f32_e32 v31, v31, v34
	v_add_f32_e32 v34, v36, v31
	v_sub_f32_e32 v30, v30, v35
	v_sub_f32_e32 v35, v34, v36
	v_ldexp_f32 v30, v30, 1
	v_sub_f32_e32 v31, v31, v35
	v_add_f32_e32 v30, v30, v31
	v_add_f32_e32 v31, v34, v30
	v_sub_f32_e32 v34, v31, v34
	v_add_f32_e32 v35, v40, v31
	v_sub_f32_e32 v30, v30, v34
	v_sub_f32_e32 v34, v35, v40
	v_sub_f32_e32 v36, v35, v34
	v_sub_f32_e32 v31, v31, v34
	v_add_f32_e32 v34, v33, v30
	v_sub_f32_e32 v36, v40, v36
	v_sub_f32_e32 v37, v34, v33
	v_add_f32_e32 v31, v31, v36
	v_sub_f32_e32 v36, v34, v37
	v_sub_f32_e32 v30, v30, v37
	v_sub_f32_e32 v33, v33, v36
	v_add_f32_e32 v31, v34, v31
	v_add_f32_e32 v30, v30, v33
	v_add_f32_e32 v33, v35, v31
	v_sub_f32_e32 v34, v33, v35
	v_sub_f32_e32 v31, v31, v34
	v_add_f32_e32 v30, v30, v31
	v_add_f32_e32 v30, v33, v30
	v_cmp_neq_f32_e32 vcc, s16, v32
	s_nop 1
	v_cndmask_b32_e32 v30, v25, v30, vcc
	v_cmp_ngt_f32_e32 vcc, -1.0, v32
	s_nop 1
	v_cndmask_b32_e32 v30, v26, v30, vcc
	v_cmp_neq_f32_e32 vcc, -1.0, v32
	s_nop 1
	v_cndmask_b32_e32 v30, v27, v30, vcc
	v_cmp_lt_f32_e64 vcc, |v32|, s17
	s_nop 1
	v_cndmask_b32_e32 v30, v30, v32, vcc
	v_sub_f32_e32 v4, v4, v30
	v_mul_f32_e32 v4, 0x3fb8aa3b, v4
	global_store_dword v[28:29], v4, off
	s_nop 1
	v_mov_b32_e32 v28, v44
	v_add_u32_e32 v4, v0, v9
	v_ashrrev_i32_e32 v5, 31, v4
	v_lshlrev_b64 v[4:5], 14, v[4:5]
	v_lshl_add_u64 v[4:5], v[18:19], 0, v[4:5]
	v_add_f32_e32 v1, v1, v28
	v_mul_f32_e64 v28, |v1|, s13
	v_exp_f32_e32 v30, v28
	v_min_f32_e32 v1, 0, v1
	v_add_f32_e32 v31, 1.0, v30
	v_add_f32_e32 v32, -1.0, v31
	v_frexp_mant_f32_e32 v33, v31
	v_cvt_f64_f32_e32 v[28:29], v31
	v_sub_f32_e32 v34, v32, v31
	v_frexp_exp_i32_f64_e32 v28, v[28:29]
	v_cmp_gt_f32_e32 vcc, s14, v33
	v_sub_f32_e32 v32, v30, v32
	v_add_f32_e32 v29, 1.0, v34
	v_subbrev_co_u32_e32 v28, vcc, 0, v28, vcc
	v_add_f32_e32 v29, v32, v29
	v_sub_u32_e32 v32, 0, v28
	v_cvt_f32_i32_e32 v28, v28
	v_ldexp_f32 v31, v31, v32
	v_ldexp_f32 v29, v29, v32
	v_add_f32_e32 v32, -1.0, v31
	v_add_f32_e32 v33, 1.0, v31
	v_add_f32_e32 v34, 1.0, v32
	v_add_f32_e32 v35, -1.0, v33
	v_sub_f32_e32 v34, v31, v34
	v_sub_f32_e32 v31, v31, v35
	v_mul_f32_e32 v35, 0x3f317218, v28
	v_add_f32_e32 v34, v29, v34
	v_add_f32_e32 v29, v29, v31
	v_fma_f32 v31, v28, s15, -v35
	v_add_f32_e32 v36, v32, v34
	v_add_f32_e32 v37, v33, v29
; __device__ __forceinline__ void fgate_groups(Frame& F, const bf16* XN, const bf16* WFT, const float* b_f, float* LOGFT) {
;     ...
;             for (int r = 0; r < 4; ++r) { const int hh = 4 * fq + r; const float z = acc[r] + b_f[hh];
;                 const float ls = fminf(z, 0.f) - log1pf(__expf(-fabsf(z)));
;                 LOGFT[(size_t)(b * NH + hh) * S + s] = ls * LOG2E; }
	v_fmac_f32_e32 v31, 0xb102e308, v28
	v_sub_f32_e32 v28, v36, v32
	v_sub_f32_e32 v32, v37, v33
	v_rcp_f32_e32 v33, v37
	v_add_f32_e32 v38, v35, v31
	v_sub_f32_e32 v29, v29, v32
	v_sub_f32_e32 v32, v38, v35
	v_sub_f32_e32 v31, v31, v32
	v_mul_f32_e32 v32, v36, v33
	v_sub_f32_e32 v28, v34, v28
	v_mul_f32_e32 v34, v37, v32
	v_fma_f32 v35, v32, v37, -v34
	v_fmac_f32_e32 v35, v32, v29
	v_add_f32_e32 v39, v34, v35
	v_sub_f32_e32 v40, v36, v39
	v_sub_f32_e32 v34, v39, v34
	v_sub_f32_e32 v36, v36, v40
	v_sub_f32_e32 v34, v34, v35
	v_sub_f32_e32 v35, v36, v39
	v_add_f32_e32 v28, v28, v35
	v_add_f32_e32 v28, v34, v28
	v_add_f32_e32 v34, v40, v28
	v_mul_f32_e32 v35, v33, v34
	v_sub_f32_e32 v36, v40, v34
	v_mul_f32_e32 v39, v37, v35
	v_add_f32_e32 v28, v28, v36
	v_add_f32_e32 v36, v32, v35
	v_fma_f32 v37, v35, v37, -v39
	v_sub_f32_e32 v32, v36, v32
	v_fmac_f32_e32 v37, v35, v29
	v_sub_f32_e32 v29, v35, v32
	v_add_f32_e32 v32, v39, v37
	v_sub_f32_e32 v35, v32, v39
	v_sub_f32_e32 v39, v34, v32
	v_sub_f32_e32 v34, v34, v39
	v_sub_f32_e32 v32, v34, v32
	v_sub_f32_e32 v35, v35, v37
	v_add_f32_e32 v28, v28, v32
	v_add_f32_e32 v28, v35, v28
	v_add_f32_e32 v28, v39, v28
	v_mul_f32_e32 v28, v33, v28
	v_add_f32_e32 v28, v29, v28
	v_add_f32_e32 v29, v36, v28
	v_mul_f32_e32 v32, v29, v29
	v_fmamk_f32 v35, v32, 0x3e9b6dac, v24
	v_sub_f32_e32 v33, v29, v36
	v_ldexp_f32 v34, v29, 1
	v_mul_f32_e32 v29, v29, v32
	v_fmaak_f32 v32, v32, v35, 0x3f2aaada
	v_mul_f32_e32 v29, v29, v32
	v_add_f32_e32 v32, v34, v29
	v_sub_f32_e32 v28, v28, v33
	v_sub_f32_e32 v33, v32, v34
	v_ldexp_f32 v28, v28, 1
	v_sub_f32_e32 v29, v29, v33
	v_add_f32_e32 v28, v28, v29
	v_add_f32_e32 v29, v32, v28
	v_sub_f32_e32 v32, v29, v32
	v_add_f32_e32 v33, v38, v29
	v_sub_f32_e32 v28, v28, v32
	v_sub_f32_e32 v32, v33, v38
	v_sub_f32_e32 v34, v33, v32
	v_sub_f32_e32 v29, v29, v32
	v_add_f32_e32 v32, v31, v28
	v_sub_f32_e32 v34, v38, v34
	v_sub_f32_e32 v35, v32, v31
	v_add_f32_e32 v29, v29, v34
	v_sub_f32_e32 v34, v32, v35
	v_sub_f32_e32 v28, v28, v35
	v_sub_f32_e32 v31, v31, v34
	v_add_f32_e32 v29, v32, v29
	v_add_f32_e32 v28, v28, v31
	v_add_f32_e32 v31, v33, v29
	v_sub_f32_e32 v32, v31, v33
	v_sub_f32_e32 v29, v29, v32
	v_add_f32_e32 v28, v28, v29
	v_add_f32_e32 v28, v31, v28
	v_cmp_neq_f32_e32 vcc, s16, v30
	s_nop 1
	v_cndmask_b32_e32 v28, v25, v28, vcc
	v_cmp_ngt_f32_e32 vcc, -1.0, v30
	s_nop 1
	v_cndmask_b32_e32 v28, v26, v28, vcc
	v_cmp_neq_f32_e32 vcc, -1.0, v30
	s_nop 1
	v_cndmask_b32_e32 v28, v27, v28, vcc
	v_cmp_lt_f32_e64 vcc, |v30|, s17
	s_nop 1
	v_cndmask_b32_e32 v28, v28, v30, vcc
	v_sub_f32_e32 v1, v1, v28
	v_mul_f32_e32 v1, 0x3fb8aa3b, v1
	global_store_dword v[4:5], v1, off
	s_nop 1
	v_mov_b32_e32 v1, v45
	v_add_u32_e32 v4, v0, v21
	v_ashrrev_i32_e32 v5, 31, v4
	v_lshlrev_b64 v[4:5], 14, v[4:5]
	v_lshl_add_u64 v[4:5], v[18:19], 0, v[4:5]
	v_add_u32_e32 v0, v0, v22
	v_add_f32_e32 v1, v2, v1
	v_mul_f32_e64 v2, |v1|, s13
	v_exp_f32_e32 v2, v2
	v_min_f32_e32 v1, 0, v1
	v_add_f32_e32 v6, 1.0, v2
	v_add_f32_e32 v30, -1.0, v6
	v_frexp_mant_f32_e32 v31, v6
	v_cvt_f64_f32_e32 v[28:29], v6
	v_sub_f32_e32 v32, v30, v6
	v_frexp_exp_i32_f64_e32 v28, v[28:29]
	v_cmp_gt_f32_e32 vcc, s14, v31
	v_sub_f32_e32 v30, v2, v30
	v_add_f32_e32 v29, 1.0, v32
	v_subbrev_co_u32_e32 v28, vcc, 0, v28, vcc
	v_add_f32_e32 v29, v30, v29
	v_sub_u32_e32 v30, 0, v28
	v_cvt_f32_i32_e32 v28, v28
	v_ldexp_f32 v6, v6, v30
	v_ldexp_f32 v29, v29, v30
	v_add_f32_e32 v30, -1.0, v6
	v_add_f32_e32 v31, 1.0, v6
	v_add_f32_e32 v32, 1.0, v30
	v_add_f32_e32 v33, -1.0, v31
	v_sub_f32_e32 v32, v6, v32
	v_sub_f32_e32 v6, v6, v33
	v_mul_f32_e32 v33, 0x3f317218, v28
	v_add_f32_e32 v32, v29, v32
	v_add_f32_e32 v6, v29, v6
	v_fma_f32 v29, v28, s15, -v33
	v_add_f32_e32 v34, v30, v32
	v_add_f32_e32 v35, v31, v6
	v_fmac_f32_e32 v29, 0xb102e308, v28
	v_sub_f32_e32 v28, v34, v30
	v_sub_f32_e32 v30, v35, v31
	v_rcp_f32_e32 v31, v35
	v_add_f32_e32 v36, v33, v29
	v_sub_f32_e32 v6, v6, v30
	v_sub_f32_e32 v30, v36, v33
	v_sub_f32_e32 v29, v29, v30
	v_mul_f32_e32 v30, v34, v31
	v_sub_f32_e32 v28, v32, v28
	v_mul_f32_e32 v32, v35, v30
	v_fma_f32 v33, v30, v35, -v32
	v_fmac_f32_e32 v33, v30, v6
	v_add_f32_e32 v37, v32, v33
	v_sub_f32_e32 v38, v34, v37
	v_sub_f32_e32 v32, v37, v32
	v_sub_f32_e32 v34, v34, v38
	v_sub_f32_e32 v32, v32, v33
	v_sub_f32_e32 v33, v34, v37
	v_add_f32_e32 v28, v28, v33
	v_add_f32_e32 v28, v32, v28
	v_add_f32_e32 v32, v38, v28
	v_mul_f32_e32 v33, v31, v32
	v_sub_f32_e32 v34, v38, v32
	v_mul_f32_e32 v37, v35, v33
	v_add_f32_e32 v28, v28, v34
	v_add_f32_e32 v34, v30, v33
	v_fma_f32 v35, v33, v35, -v37
	v_sub_f32_e32 v30, v34, v30
	v_fmac_f32_e32 v35, v33, v6
	v_sub_f32_e32 v6, v33, v30
	v_add_f32_e32 v30, v37, v35
	v_sub_f32_e32 v33, v30, v37
	v_sub_f32_e32 v37, v32, v30
	v_sub_f32_e32 v32, v32, v37
	v_sub_f32_e32 v30, v32, v30
	v_sub_f32_e32 v33, v33, v35
	v_add_f32_e32 v28, v28, v30
	v_add_f32_e32 v28, v33, v28
	v_add_f32_e32 v28, v37, v28
	v_mul_f32_e32 v28, v31, v28
	v_add_f32_e32 v6, v6, v28
; __device__ __forceinline__ void fgate_groups(Frame& F, const bf16* XN, const bf16* WFT, const float* b_f, float* LOGFT) {
;     ...
;             for (int r = 0; r < 4; ++r) { const int hh = 4 * fq + r; const float z = acc[r] + b_f[hh];
;                 const float ls = fminf(z, 0.f) - log1pf(__expf(-fabsf(z)));
;                 LOGFT[(size_t)(b * NH + hh) * S + s] = ls * LOG2E; }
	v_add_f32_e32 v28, v34, v6
	v_mul_f32_e32 v30, v28, v28
	v_fmamk_f32 v33, v30, 0x3e9b6dac, v24
	v_sub_f32_e32 v31, v28, v34
	v_ldexp_f32 v32, v28, 1
	v_mul_f32_e32 v28, v28, v30
	v_fmaak_f32 v30, v30, v33, 0x3f2aaada
	v_mul_f32_e32 v28, v28, v30
	v_add_f32_e32 v30, v32, v28
	v_sub_f32_e32 v6, v6, v31
	v_sub_f32_e32 v31, v30, v32
	v_ldexp_f32 v6, v6, 1
	v_sub_f32_e32 v28, v28, v31
	v_add_f32_e32 v6, v6, v28
	v_add_f32_e32 v28, v30, v6
	v_sub_f32_e32 v30, v28, v30
	v_add_f32_e32 v31, v36, v28
	v_sub_f32_e32 v6, v6, v30
	v_sub_f32_e32 v30, v31, v36
	v_sub_f32_e32 v32, v31, v30
	v_sub_f32_e32 v28, v28, v30
	v_add_f32_e32 v30, v29, v6
	v_sub_f32_e32 v32, v36, v32
	v_sub_f32_e32 v33, v30, v29
	v_add_f32_e32 v28, v28, v32
	v_sub_f32_e32 v32, v30, v33
	v_sub_f32_e32 v6, v6, v33
	v_sub_f32_e32 v29, v29, v32
	v_add_f32_e32 v28, v30, v28
	v_add_f32_e32 v6, v6, v29
	v_add_f32_e32 v29, v31, v28
	v_sub_f32_e32 v30, v29, v31
	v_sub_f32_e32 v28, v28, v30
	v_add_f32_e32 v6, v6, v28
	v_add_f32_e32 v6, v29, v6
	v_cmp_neq_f32_e32 vcc, s16, v2
	s_nop 1
	v_cndmask_b32_e32 v6, v25, v6, vcc
	v_cmp_ngt_f32_e32 vcc, -1.0, v2
	s_nop 1
	v_cndmask_b32_e32 v6, v26, v6, vcc
	v_cmp_neq_f32_e32 vcc, -1.0, v2
	s_nop 1
	v_cndmask_b32_e32 v6, v27, v6, vcc
	v_cmp_lt_f32_e64 vcc, |v2|, s17
	s_nop 1
	v_cndmask_b32_e32 v2, v6, v2, vcc
	v_sub_f32_e32 v1, v1, v2
	v_mul_f32_e32 v1, 0x3fb8aa3b, v1
	global_store_dword v[4:5], v1, off
	s_nop 1
	v_mov_b32_e32 v1, v46
	v_add_f32_e32 v2, v3, v7
	v_add_f32_e32 v2, v2, v1
	v_mul_f32_e64 v1, |v2|, s13
	v_exp_f32_e32 v4, v1
	v_min_f32_e32 v5, 0, v2
	v_ashrrev_i32_e32 v1, 31, v0
	v_lshlrev_b64 v[0:1], 14, v[0:1]
	v_add_f32_e32 v6, 1.0, v4
	v_add_f32_e32 v7, -1.0, v6
	v_frexp_mant_f32_e32 v28, v6
	v_cvt_f64_f32_e32 v[2:3], v6
	v_sub_f32_e32 v29, v7, v6
	v_frexp_exp_i32_f64_e32 v2, v[2:3]
	v_cmp_gt_f32_e32 vcc, s14, v28
	v_sub_f32_e32 v7, v4, v7
	v_add_f32_e32 v3, 1.0, v29
	v_subbrev_co_u32_e32 v2, vcc, 0, v2, vcc
	v_add_f32_e32 v3, v7, v3
	v_sub_u32_e32 v7, 0, v2
	v_cvt_f32_i32_e32 v2, v2
	v_ldexp_f32 v6, v6, v7
	v_ldexp_f32 v3, v3, v7
	v_add_f32_e32 v7, -1.0, v6
	v_add_f32_e32 v28, 1.0, v6
	v_add_f32_e32 v29, 1.0, v7
	v_add_f32_e32 v30, -1.0, v28
	v_sub_f32_e32 v29, v6, v29
	v_sub_f32_e32 v6, v6, v30
	v_mul_f32_e32 v30, 0x3f317218, v2
	v_add_f32_e32 v29, v3, v29
	v_add_f32_e32 v3, v3, v6
	v_fma_f32 v6, v2, s15, -v30
	v_add_f32_e32 v31, v7, v29
	v_add_f32_e32 v32, v28, v3
	v_fmac_f32_e32 v6, 0xb102e308, v2
	v_sub_f32_e32 v2, v31, v7
	v_sub_f32_e32 v7, v32, v28
	v_rcp_f32_e32 v28, v32
	v_add_f32_e32 v33, v30, v6
	v_sub_f32_e32 v3, v3, v7
	v_sub_f32_e32 v7, v33, v30
	v_sub_f32_e32 v6, v6, v7
	v_mul_f32_e32 v7, v31, v28
	v_sub_f32_e32 v2, v29, v2
	v_mul_f32_e32 v29, v32, v7
	v_fma_f32 v30, v7, v32, -v29
	v_fmac_f32_e32 v30, v7, v3
	v_add_f32_e32 v34, v29, v30
	v_sub_f32_e32 v35, v31, v34
	v_sub_f32_e32 v29, v34, v29
	v_sub_f32_e32 v31, v31, v35
	v_sub_f32_e32 v29, v29, v30
	v_sub_f32_e32 v30, v31, v34
	v_add_f32_e32 v2, v2, v30
	v_add_f32_e32 v2, v29, v2
	v_add_f32_e32 v29, v35, v2
	v_mul_f32_e32 v30, v28, v29
	v_sub_f32_e32 v31, v35, v29
	v_mul_f32_e32 v34, v32, v30
	v_add_f32_e32 v2, v2, v31
	v_add_f32_e32 v31, v7, v30
	v_fma_f32 v32, v30, v32, -v34
	v_sub_f32_e32 v7, v31, v7
	v_fmac_f32_e32 v32, v30, v3
	v_sub_f32_e32 v3, v30, v7
	v_add_f32_e32 v7, v34, v32
	v_sub_f32_e32 v30, v7, v34
	v_sub_f32_e32 v34, v29, v7
	v_sub_f32_e32 v29, v29, v34
	v_sub_f32_e32 v7, v29, v7
	v_sub_f32_e32 v30, v30, v32
	v_add_f32_e32 v2, v2, v7
	v_add_f32_e32 v2, v30, v2
	v_add_f32_e32 v2, v34, v2
	v_mul_f32_e32 v2, v28, v2
	v_add_f32_e32 v2, v3, v2
	v_add_f32_e32 v3, v31, v2
	v_mul_f32_e32 v7, v3, v3
	v_fmamk_f32 v30, v7, 0x3e9b6dac, v24
	v_sub_f32_e32 v28, v3, v31
	v_ldexp_f32 v29, v3, 1
	v_mul_f32_e32 v3, v3, v7
	v_fmaak_f32 v7, v7, v30, 0x3f2aaada
	v_mul_f32_e32 v3, v3, v7
	v_add_f32_e32 v7, v29, v3
	v_sub_f32_e32 v2, v2, v28
	v_sub_f32_e32 v28, v7, v29
	v_ldexp_f32 v2, v2, 1
	v_sub_f32_e32 v3, v3, v28
	v_add_f32_e32 v2, v2, v3
	v_add_f32_e32 v3, v7, v2
	v_sub_f32_e32 v7, v3, v7
	v_add_f32_e32 v28, v33, v3
	v_sub_f32_e32 v2, v2, v7
	v_sub_f32_e32 v7, v28, v33
	v_sub_f32_e32 v29, v28, v7
	v_sub_f32_e32 v3, v3, v7
	v_add_f32_e32 v7, v6, v2
	v_sub_f32_e32 v29, v33, v29
	v_sub_f32_e32 v30, v7, v6
	v_add_f32_e32 v3, v3, v29
	v_sub_f32_e32 v29, v7, v30
	v_sub_f32_e32 v2, v2, v30
	v_sub_f32_e32 v6, v6, v29
	v_add_f32_e32 v3, v7, v3
	v_add_f32_e32 v2, v2, v6
	v_add_f32_e32 v6, v28, v3
	v_sub_f32_e32 v7, v6, v28
	v_sub_f32_e32 v3, v3, v7
	v_add_f32_e32 v2, v2, v3
	v_add_f32_e32 v2, v6, v2
	v_cmp_neq_f32_e32 vcc, s16, v4
	v_lshl_add_u64 v[0:1], v[18:19], 0, v[0:1]
	s_nop 0
	v_cndmask_b32_e32 v2, v25, v2, vcc
	v_cmp_ngt_f32_e32 vcc, -1.0, v4
	s_nop 1
	v_cndmask_b32_e32 v2, v26, v2, vcc
	v_cmp_neq_f32_e32 vcc, -1.0, v4
	s_nop 1
	v_cndmask_b32_e32 v2, v27, v2, vcc
	v_cmp_lt_f32_e64 vcc, |v4|, s17
	s_nop 1
	v_cndmask_b32_e32 v2, v2, v4, vcc
	v_sub_f32_e32 v2, v5, v2
	v_mul_f32_e32 v2, 0x3fb8aa3b, v2
	global_store_dword v[0:1], v2, off
	s_branch .LBB0_219

; __device__ __forceinline__ int pg8_lane_id() { int l; asm volatile("v_mbcnt_lo_u32_b32 %0, -1, 0\n\tv_mbcnt_hi_u32_b32 %0, -1, %0" : "=v"(l)); return l; }
; #define LAS __attribute__((address_space(3)))
; __global__ void __launch_bounds__(NWAVES * 64, 2) mk_fwd(Args args) {
;     ...
;     if (IN(13) || IN(14) || IN(15)) {
;         volatile LAS int* tab = (volatile LAS int*)(F.lds + TAB_OFF);
;         if (F.wave == 0 && pg8::pg8_lane_id() == 0) { int accp = 0;
;             for (int e = 0; e < NE; ++e) { const int n = (int)__hip_atomic_load(F.ctl + CW_CNT + 64 * e, RLX_AGENT); tab[e] = accp; accp += (n + 255) >> 8; }
;             tab[8] = accp; }
;         __syncthreads();
;     }
.LBB0_1737:
	s_and_b64 vcc, exec, s[4:5]
	s_cbranch_vccz .LBB0_1743
	s_and_b64 vcc, exec, s[56:57]
	s_cbranch_vccnz .LBB0_1742
	v_mbcnt_lo_u32_b32 v0, -1, 0
	v_mbcnt_hi_u32_b32 v0, -1, v0
	s_nop 0
	v_cmp_eq_u32_e32 vcc, 0, v0
	s_and_saveexec_b64 s[4:5], vcc
	s_cbranch_execz .LBB0_1741
	s_add_i32 s3, 0, 0x201c0
	v_mov_b32_e32 v0, 0x10000
	v_mov_b32_e32 v9, s3
	v_mov_b32_e32 v10, 0
	s_waitcnt lgkmcnt(0)
	global_load_dword v1, v0, s[78:79] sc1
	global_load_dword v2, v0, s[78:79] offset:256 sc1
	global_load_dword v3, v0, s[78:79] offset:512 sc1
	global_load_dword v4, v0, s[78:79] offset:768 sc1
	global_load_dword v5, v0, s[78:79] offset:1024 sc1
	global_load_dword v6, v0, s[78:79] offset:1280 sc1
	global_load_dword v7, v0, s[78:79] offset:1536 sc1
	global_load_dword v8, v0, s[78:79] offset:1792 sc1
	ds_write_b32 v9, v10
	s_waitcnt vmcnt(7)
	v_add_u32_e32 v1, 0xff, v1
	v_ashrrev_i32_e32 v1, 8, v1
	ds_write_b32 v9, v1 offset:4
	s_waitcnt vmcnt(6)
	v_add_u32_e32 v2, 0xff, v2
	v_ashrrev_i32_e32 v2, 8, v2
	v_add_u32_e32 v1, v2, v1
	ds_write_b32 v9, v1 offset:8
	s_waitcnt vmcnt(5)
	v_add_u32_e32 v3, 0xff, v3
	v_ashrrev_i32_e32 v3, 8, v3
	v_add_u32_e32 v1, v3, v1
	ds_write_b32 v9, v1 offset:12
	s_waitcnt vmcnt(4)
	v_add_u32_e32 v4, 0xff, v4
	v_ashrrev_i32_e32 v4, 8, v4
	v_add_u32_e32 v1, v4, v1
	ds_write_b32 v9, v1 offset:16
	s_waitcnt vmcnt(3)
	v_add_u32_e32 v5, 0xff, v5
	v_ashrrev_i32_e32 v5, 8, v5
	v_add_u32_e32 v1, v5, v1
	ds_write_b32 v9, v1 offset:20
	s_waitcnt vmcnt(2)
	v_add_u32_e32 v6, 0xff, v6
	v_ashrrev_i32_e32 v6, 8, v6
	v_add_u32_e32 v1, v6, v1
	ds_write_b32 v9, v1 offset:24
	s_waitcnt vmcnt(1)
	v_add_u32_e32 v7, 0xff, v7
	v_ashrrev_i32_e32 v7, 8, v7
	v_add_u32_e32 v1, v7, v1
	ds_write_b32 v9, v1 offset:28
	s_waitcnt vmcnt(0)
	v_add_u32_e32 v8, 0xff, v8
	v_ashrrev_i32_e32 v8, 8, v8
	v_add_u32_e32 v1, v8, v1
	ds_write_b32 v9, v1 offset:32

; #define GAS __attribute__((address_space(1)))
; __device__ __forceinline__ float bf_lo(unsigned w) { return __uint_as_float(w << 16); }
; __device__ __forceinline__ float bf_hi(unsigned w) { return __uint_as_float(w & 0xffff0000u); }
; __device__ __forceinline__ void final_rows(Frame& F, const bf16* XA, const bf16* YS, const int* posi, const float* wl, const float* PART, const LAS int* tab, const float* gate, const float* g, float* out) {
;     ...
;     for (int rg = gw; rg < M / 8; rg += NGW) {
;         const int row0 = rg * 8, b = row0 / S;
;         f32x4 gt[4], gf[4];
; #pragma unroll
;         for (int j = 0; j < 4; ++j) { gt[j] = ((const GAS f32x4*)(gate + (size_t)b * NMOD))[lane + 64 * j]; gf[j] = ((const GAS f32x4*)g)[lane + 64 * j]; }
; #pragma unroll 2
;         for (int r = 0; r < 8; ++r) {
;             const int row = row0 + r;
;             const GAS unsigned long long* xr = (const GAS unsigned long long*)(XA + (size_t)row * D) + lane;
;             const int d0 = __builtin_amdgcn_readfirstlane(posi[2 * row]), d1 = __builtin_amdgcn_readfirstlane(posi[2 * row + 1]);
;             const float w0 = __builtin_bit_cast(float, __builtin_amdgcn_readfirstlane(__builtin_bit_cast(int, wl[d0]))), w1 = __builtin_bit_cast(float, __builtin_amdgcn_readfirstlane(__builtin_bit_cast(int, wl[d1])));
;             const int c0 = __builtin_amdgcn_readfirstlane(tab[d0 >> 14]) * 256 + (d0 & (ECAP - 1)), c1 = __builtin_amdgcn_readfirstlane(tab[d1 >> 14]) * 256 + (d1 & (ECAP - 1));
;             f32x4 ys[4];
;     ...
;             for (int j = 0; j < 4; ++j) { const unsigned long long xq = xr[64 * j]; const unsigned xl = (unsigned)xq, xh = (unsigned)(xq >> 32);
;                 v[j] = (f32x4){bf_lo(xl), bf_hi(xl), bf_lo(xh), bf_hi(xh)} + gt[j] * ys[j]; s += (v[j].x * v[j].x + v[j].y * v[j].y) + (v[j].z * v[j].z + v[j].w * v[j].w); }
;             const float rstd = rsqrtf(wave_sum(s) * (1.f / D) + RMS_EPS);
;             GAS f32x4* o = (GAS f32x4*)(out + (size_t)row * D) + lane;
; #pragma unroll
;             for (int j = 0; j < 4; ++j) o[64 * j] = v[j] * rstd * gf[j];
.LBB0_1947:
	s_ashr_i32 s0, s7, 31
	s_lshr_b32 s0, s0, 23
	s_add_i32 s0, s7, s0
	s_ashr_i32 s0, s0, 9
	v_mad_i64_i32 v[0:1], s[2:3], s0, v83, v[62:63]
	s_lshl_b32 s34, s7, 6
	s_add_u32 s34, s20, s34
	s_addc_u32 s35, s21, 0
	global_load_dwordx4 v[202:205], v84, s[34:35]
	global_load_dwordx4 v[16:19], v[0:1], off
	global_load_dwordx4 v[20:23], v[0:1], off offset:1024
	global_load_dwordx4 v[24:27], v[52:53], off
	global_load_dwordx4 v[28:31], v[52:53], off offset:1024
	global_load_dwordx4 v[32:35], v[0:1], off offset:2048
	global_load_dwordx4 v[36:39], v[0:1], off offset:3072
	global_load_dwordx4 v[40:43], v[52:53], off offset:2048
	global_load_dwordx4 v[44:47], v[52:53], off offset:3072
	s_waitcnt vmcnt(8)
	s_lshl_b32 s25, s7, 3
	s_mov_b32 s26, s1
	s_branch .LBB0_1949
.LBB0_1948:
	s_ashr_i32 s3, s2, 31
	s_lshl_b64 s[4:5], s[2:3], 11
	s_add_i32 s26, s26, 2
	s_lshl_b64 s[2:3], s[2:3], 12
	s_cmp_eq_u32 s26, 8
	v_lshlrev_b32_e32 v12, 16, v194
	v_and_b32_e32 v13, 0xffff0000, v194
	v_lshlrev_b32_e32 v14, 16, v195
	v_and_b32_e32 v15, 0xffff0000, v195
	v_lshlrev_b32_e32 v70, 16, v196
	v_and_b32_e32 v71, 0xffff0000, v196
	v_lshlrev_b32_e32 v64, 16, v197
	v_and_b32_e32 v65, 0xffff0000, v197
	v_lshlrev_b32_e32 v72, 16, v198
	v_and_b32_e32 v73, 0xffff0000, v198
	v_lshlrev_b32_e32 v66, 16, v199
	v_and_b32_e32 v67, 0xffff0000, v199
	v_lshlrev_b32_e32 v76, 16, v200
	v_and_b32_e32 v77, 0xffff0000, v200
	v_lshlrev_b32_e32 v68, 16, v201
	v_and_b32_e32 v69, 0xffff0000, v201
	v_pk_fma_f32 v[0:1], v[16:17], v[0:1], v[12:13]
	v_pk_fma_f32 v[2:3], v[18:19], v[2:3], v[14:15]
	v_pk_fma_f32 v[4:5], v[20:21], v[4:5], v[70:71]
	v_pk_fma_f32 v[6:7], v[22:23], v[6:7], v[64:65]
	v_pk_fma_f32 v[10:11], v[34:35], v[10:11], v[66:67]
	v_pk_fma_f32 v[12:13], v[38:39], v[50:51], v[68:69]
	v_pk_fma_f32 v[14:15], v[36:37], v[48:49], v[76:77]
	v_pk_mul_f32 v[48:49], v[2:3], v[2:3]
	v_pk_mul_f32 v[50:51], v[0:1], v[0:1]
	v_pk_mul_f32 v[64:65], v[6:7], v[6:7]
	v_pk_mul_f32 v[66:67], v[4:5], v[4:5]
	v_pk_fma_f32 v[8:9], v[32:33], v[8:9], v[72:73]
	v_pk_mov_b32 v[72:73], v[50:51], v[48:49] op_sel:[1,0]
	v_mov_b32_e32 v51, v49
	v_pk_mov_b32 v[48:49], v[66:67], v[64:65] op_sel:[1,0]
	v_mov_b32_e32 v67, v65
	v_mul_f32_e32 v71, v14, v14
	v_mul_f32_e32 v68, v9, v9
	v_mul_f32_e32 v70, v11, v11
	v_pk_add_f32 v[50:51], v[72:73], v[50:51]
	v_pk_add_f32 v[48:49], v[48:49], v[66:67]
	v_mul_f32_e32 v74, v15, v15
	v_mul_f32_e32 v76, v12, v12
	v_mul_f32_e32 v77, v13, v13
	v_pk_fma_f32 v[64:65], v[8:9], v[8:9], v[68:69] op_sel_hi:[1,1,0]
	v_pk_fma_f32 v[68:69], v[10:11], v[10:11], v[70:71] op_sel_hi:[1,1,0]
	v_pk_add_f32 v[50:51], v[50:51], v[50:51] op_sel:[0,1] op_sel_hi:[1,0]
	v_pk_add_f32 v[48:49], v[48:49], v[48:49] op_sel:[0,1] op_sel_hi:[1,0]
	v_mov_b32_e32 v65, v76
	v_mov_b32_e32 v69, v77
	v_mov_b32_e32 v51, v71
	v_mov_b32_e32 v49, v74
	v_pk_add_f32 v[64:65], v[64:65], v[68:69]
	v_pk_add_f32 v[48:49], v[50:51], v[48:49]
	s_nop 0
	v_pk_add_f32 v[48:49], v[48:49], v[64:65]
	s_nop 0
	v_add_f32_e32 v48, v48, v49
	ds_bpermute_b32 v49, v75, v48
	s_waitcnt lgkmcnt(0)
	v_add_f32_e32 v48, v48, v49
	ds_bpermute_b32 v49, v78, v48
	s_waitcnt lgkmcnt(0)
	v_add_f32_e32 v48, v48, v49
	ds_bpermute_b32 v49, v79, v48
	s_waitcnt lgkmcnt(0)
	v_add_f32_e32 v48, v48, v49
	ds_bpermute_b32 v49, v80, v48
	s_waitcnt lgkmcnt(0)
	v_add_f32_e32 v48, v48, v49
	ds_bpermute_b32 v49, v81, v48
	s_waitcnt lgkmcnt(0)
	v_add_f32_e32 v48, v48, v49
	ds_bpermute_b32 v49, v82, v48
	s_waitcnt lgkmcnt(0)
	v_add_f32_e32 v48, v48, v49
	v_fmamk_f32 v48, v48, 0x3a800000, v85
	v_mul_f32_e32 v49, 0x4b800000, v48
	v_cmp_gt_f32_e32 vcc, s19, v48
	s_nop 1
	v_cndmask_b32_e32 v48, v48, v49, vcc
	v_rsq_f32_e32 v50, v48
	v_lshl_add_u64 v[48:49], v[60:61], 0, s[2:3]
	v_mul_f32_e32 v51, 0x45800000, v50
	v_cndmask_b32_e32 v50, v50, v51, vcc
	v_pk_mul_f32 v[0:1], v[0:1], v[50:51] op_sel_hi:[1,0]
	v_pk_mul_f32 v[2:3], v[2:3], v[50:51] op_sel_hi:[1,0]
	v_pk_mul_f32 v[4:5], v[4:5], v[50:51] op_sel_hi:[1,0]
	v_pk_mul_f32 v[6:7], v[6:7], v[50:51] op_sel_hi:[1,0]
	v_pk_mul_f32 v[8:9], v[8:9], v[50:51] op_sel_hi:[1,0]
	v_pk_mul_f32 v[10:11], v[10:11], v[50:51] op_sel_hi:[1,0]
	v_pk_mul_f32 v[64:65], v[14:15], v[50:51] op_sel_hi:[1,0]
	v_pk_mul_f32 v[12:13], v[12:13], v[50:51] op_sel_hi:[1,0]
	v_pk_mul_f32 v[2:3], v[26:27], v[2:3]
	v_pk_mul_f32 v[0:1], v[24:25], v[0:1]
	v_pk_mul_f32 v[6:7], v[30:31], v[6:7]
	v_pk_mul_f32 v[4:5], v[28:29], v[4:5]
	v_pk_mul_f32 v[10:11], v[42:43], v[10:11]
	v_pk_mul_f32 v[8:9], v[40:41], v[8:9]
	v_pk_mul_f32 v[14:15], v[46:47], v[12:13]
	v_pk_mul_f32 v[12:13], v[44:45], v[64:65]
	global_store_dwordx4 v[48:49], v[0:3], off
	global_store_dwordx4 v[48:49], v[4:7], off offset:1024
	global_store_dwordx4 v[48:49], v[8:11], off offset:2048
	global_store_dwordx4 v[48:49], v[12:15], off offset:3072
	v_mov_b32_e32 v202, v206
	v_mov_b32_e32 v203, v207
	v_mov_b32_e32 v204, v208
	v_mov_b32_e32 v205, v209
	s_cbranch_scc1 .LBB0_1946
; #define GAS __attribute__((address_space(1)))
; __device__ __forceinline__ void final_rows(Frame& F, const bf16* XA, const bf16* YS, const int* posi, const float* wl, const float* PART, const LAS int* tab, const float* gate, const float* g, float* out) {
;     ...
;         for (int r = 0; r < 8; ++r) {
;             const int row = row0 + r;
;             const GAS unsigned long long* xr = (const GAS unsigned long long*)(XA + (size_t)row * D) + lane;
;             const int d0 = __builtin_amdgcn_readfirstlane(posi[2 * row]), d1 = __builtin_amdgcn_readfirstlane(posi[2 * row + 1]);
;             const float w0 = __builtin_bit_cast(float, __builtin_amdgcn_readfirstlane(__builtin_bit_cast(int, wl[d0]))), w1 = __builtin_bit_cast(float, __builtin_amdgcn_readfirstlane(__builtin_bit_cast(int, wl[d1])));
;             const int c0 = __builtin_amdgcn_readfirstlane(tab[d0 >> 14]) * 256 + (d0 & (ECAP - 1)), c1 = __builtin_amdgcn_readfirstlane(tab[d1 >> 14]) * 256 + (d1 & (ECAP - 1));
;             f32x4 ys[4];
;             if (c0 < pg8::TAIL_M0 * 256 && c1 < pg8::TAIL_M0 * 256) {
.LBB0_1949:
	s_add_i32 s4, s26, s25
	s_add_u32 s34, s34, 16
	s_addc_u32 s35, s35, 0
	global_load_dwordx4 v[206:209], v84, s[34:35]
	s_ashr_i32 s5, s4, 31
	s_lshl_b64 s[36:37], s[4:5], 11
	v_lshl_add_u64 v[214:215], v[54:55], 0, s[36:37]
	global_load_dwordx2 v[186:187], v[214:215], off
	global_load_dwordx2 v[188:189], v[214:215], off offset:512
	global_load_dwordx2 v[190:191], v[214:215], off offset:1024
	global_load_dwordx2 v[192:193], v[214:215], off offset:1536
	global_load_dwordx2 v[194:195], v[214:215], off offset:2048
	global_load_dwordx2 v[196:197], v[214:215], off offset:2560
	global_load_dwordx2 v[198:199], v[214:215], off offset:3072
	global_load_dwordx2 v[200:201], v[214:215], off offset:3584
	v_readfirstlane_b32 s38, v204
	v_readfirstlane_b32 s39, v205
	s_mov_b32 s40, s38
	s_ashr_i32 s41, s38, 31
	s_lshl_b64 s[40:41], s[40:41], 2
	s_add_u32 s40, s22, s40
	s_addc_u32 s41, s23, s41
	s_mov_b32 s42, s39
	s_ashr_i32 s43, s39, 31
	s_lshl_b64 s[42:43], s[42:43], 2
	s_add_u32 s42, s22, s42
	s_addc_u32 s43, s23, s43
	global_load_dword v212, v84, s[40:41]
	global_load_dword v213, v84, s[42:43]
	v_readfirstlane_b32 s2, v202
	s_ashr_i32 s3, s2, 31
	s_lshl_b64 s[10:11], s[2:3], 2
	v_readfirstlane_b32 s8, v203
	s_add_u32 s10, s22, s10
	s_addc_u32 s11, s23, s11
	s_ashr_i32 s9, s8, 31
	s_lshl_b64 s[12:13], s[8:9], 2
	s_add_u32 s12, s22, s12
	s_addc_u32 s13, s23, s13
	global_load_dword v0, v84, s[10:11]
	global_load_dword v1, v84, s[12:13]
	s_ashr_i32 s0, s2, 14
	s_ashr_i32 s3, s8, 14
	s_lshl_b32 s0, s0, 2
	s_lshl_b32 s3, s3, 2
	s_add_i32 s0, s18, s0
	s_add_i32 s3, s18, s3
	v_mov_b32_e32 v2, s0
	v_mov_b32_e32 v3, s3
	ds_read_b32 v2, v2
	ds_read_b32 v3, v3
	s_and_b32 s0, s2, 0x3fff
	s_and_b32 s2, s8, 0x3fff
	s_mov_b64 s[12:13], -1
	s_waitcnt lgkmcnt(1)
	v_readfirstlane_b32 s3, v2
	s_waitcnt lgkmcnt(0)
	v_readfirstlane_b32 s5, v3
	s_lshl_b32 s3, s3, 8
	s_lshl_b32 s5, s5, 8
	s_add_i32 s10, s3, s0
	s_add_i32 s8, s5, s2
	s_max_i32 s0, s10, s8
	s_cmp_lt_i32 s0, 0x8000
	s_waitcnt vmcnt(1)
	v_readfirstlane_b32 s2, v0
	s_waitcnt vmcnt(0)
	v_readfirstlane_b32 s6, v1
	s_cbranch_scc1 .LBB0_1957
	v_mov_b32_e32 v48, 0
	v_mov_b32_e32 v49, v48
	v_mov_b32_e32 v50, v48
	v_mov_b32_e32 v51, v48
	v_mov_b32_e32 v0, v48
	v_mov_b32_e32 v1, v48
	v_mov_b32_e32 v64, v48
	v_mov_b32_e32 v65, v48
	v_mov_b32_e32 v66, v48
	v_mov_b32_e32 v67, v48
	v_mov_b32_e32 v68, v48
	v_mov_b32_e32 v69, v48
	v_mov_b32_e32 v70, v48
	v_mov_b32_e32 v71, v48
	v_mov_b32_e32 v72, v48
	v_mov_b32_e32 v73, v48

; #define GAS __attribute__((address_space(1)))
; __device__ __forceinline__ float bf_lo(unsigned w) { return __uint_as_float(w << 16); }
; __device__ __forceinline__ float bf_hi(unsigned w) { return __uint_as_float(w & 0xffff0000u); }
; __device__ __forceinline__ void final_rows(Frame& F, const bf16* XA, const bf16* YS, const int* posi, const float* wl, const float* PART, const LAS int* tab, const float* gate, const float* g, float* out) {
;     ...
;             const int row = row0 + r;
;             const GAS unsigned long long* xr = (const GAS unsigned long long*)(XA + (size_t)row * D) + lane;
;             const int d0 = __builtin_amdgcn_readfirstlane(posi[2 * row]), d1 = __builtin_amdgcn_readfirstlane(posi[2 * row + 1]);
;             const float w0 = __builtin_bit_cast(float, __builtin_amdgcn_readfirstlane(__builtin_bit_cast(int, wl[d0]))), w1 = __builtin_bit_cast(float, __builtin_amdgcn_readfirstlane(__builtin_bit_cast(int, wl[d1])));
;             const int c0 = __builtin_amdgcn_readfirstlane(tab[d0 >> 14]) * 256 + (d0 & (ECAP - 1)), c1 = __builtin_amdgcn_readfirstlane(tab[d1 >> 14]) * 256 + (d1 & (ECAP - 1));
;             f32x4 ys[4];
;             if (c0 < pg8::TAIL_M0 * 256 && c1 < pg8::TAIL_M0 * 256) {
;     ...
;             f32x4 v[4]; float s = 0.f;
; #pragma unroll
;             for (int j = 0; j < 4; ++j) { const unsigned long long xq = xr[64 * j]; const unsigned xl = (unsigned)xq, xh = (unsigned)(xq >> 32);
;                 v[j] = (f32x4){bf_lo(xl), bf_hi(xl), bf_lo(xh), bf_hi(xh)} + gt[j] * ys[j]; s += (v[j].x * v[j].x + v[j].y * v[j].y) + (v[j].z * v[j].z + v[j].w * v[j].w); }
;             const float rstd = rsqrtf(wave_sum(s) * (1.f / D) + RMS_EPS);
;             GAS f32x4* o = (GAS f32x4*)(out + (size_t)row * D) + lane;
; #pragma unroll
;             for (int j = 0; j < 4; ++j) o[64 * j] = v[j] * rstd * gf[j];
.LBB0_1959:
	s_ashr_i32 s5, s4, 31
	s_lshl_b64 s[2:3], s[4:5], 11
	s_add_i32 s2, s4, 1
	s_lshl_b32 s8, s2, 1
	s_lshl_b64 s[4:5], s[4:5], 12
	s_ashr_i32 s9, s8, 31
	v_lshlrev_b32_e32 v12, 16, v186
	v_and_b32_e32 v13, 0xffff0000, v186
	v_lshlrev_b32_e32 v14, 16, v187
	v_and_b32_e32 v15, 0xffff0000, v187
	v_lshlrev_b32_e32 v70, 16, v188
	v_and_b32_e32 v71, 0xffff0000, v188
	v_lshlrev_b32_e32 v64, 16, v189
	v_and_b32_e32 v65, 0xffff0000, v189
	v_lshlrev_b32_e32 v72, 16, v190
	v_and_b32_e32 v73, 0xffff0000, v190
	v_lshlrev_b32_e32 v66, 16, v191
	v_and_b32_e32 v67, 0xffff0000, v191
	v_lshlrev_b32_e32 v76, 16, v192
	v_and_b32_e32 v77, 0xffff0000, v192
	v_lshlrev_b32_e32 v68, 16, v193
	v_and_b32_e32 v69, 0xffff0000, v193
	v_pk_fma_f32 v[0:1], v[16:17], v[0:1], v[12:13]
	v_pk_fma_f32 v[2:3], v[18:19], v[2:3], v[14:15]
	v_pk_fma_f32 v[4:5], v[20:21], v[4:5], v[70:71]
	v_pk_fma_f32 v[6:7], v[22:23], v[6:7], v[64:65]
	v_pk_fma_f32 v[10:11], v[34:35], v[10:11], v[66:67]
	v_pk_fma_f32 v[12:13], v[38:39], v[50:51], v[68:69]
	v_pk_fma_f32 v[14:15], v[36:37], v[48:49], v[76:77]
	v_pk_mul_f32 v[48:49], v[2:3], v[2:3]
	v_pk_mul_f32 v[50:51], v[0:1], v[0:1]
	v_pk_mul_f32 v[64:65], v[6:7], v[6:7]
	v_pk_mul_f32 v[66:67], v[4:5], v[4:5]
	v_pk_fma_f32 v[8:9], v[32:33], v[8:9], v[72:73]
	v_pk_mov_b32 v[72:73], v[50:51], v[48:49] op_sel:[1,0]
	v_mov_b32_e32 v51, v49
	v_pk_mov_b32 v[48:49], v[66:67], v[64:65] op_sel:[1,0]
	v_mov_b32_e32 v67, v65
	v_mul_f32_e32 v71, v14, v14
	v_mul_f32_e32 v68, v9, v9
	v_mul_f32_e32 v70, v11, v11
	v_pk_add_f32 v[50:51], v[72:73], v[50:51]
	v_pk_add_f32 v[48:49], v[48:49], v[66:67]
	v_mul_f32_e32 v74, v15, v15
	v_mul_f32_e32 v76, v12, v12
	v_mul_f32_e32 v77, v13, v13
	v_pk_fma_f32 v[64:65], v[8:9], v[8:9], v[68:69] op_sel_hi:[1,1,0]
	v_pk_fma_f32 v[68:69], v[10:11], v[10:11], v[70:71] op_sel_hi:[1,1,0]
	v_pk_add_f32 v[50:51], v[50:51], v[50:51] op_sel:[0,1] op_sel_hi:[1,0]
	v_pk_add_f32 v[48:49], v[48:49], v[48:49] op_sel:[0,1] op_sel_hi:[1,0]
	v_mov_b32_e32 v65, v76
	v_mov_b32_e32 v69, v77
	v_mov_b32_e32 v51, v71
	v_mov_b32_e32 v49, v74
	v_pk_add_f32 v[64:65], v[64:65], v[68:69]
	v_pk_add_f32 v[48:49], v[50:51], v[48:49]
	s_nop 0
	v_pk_add_f32 v[48:49], v[48:49], v[64:65]
	s_nop 0
	v_add_f32_e32 v48, v48, v49
	ds_bpermute_b32 v49, v75, v48
	s_waitcnt lgkmcnt(0)
	v_add_f32_e32 v48, v48, v49
	ds_bpermute_b32 v49, v78, v48
	s_waitcnt lgkmcnt(0)
	v_add_f32_e32 v48, v48, v49
	ds_bpermute_b32 v49, v79, v48
	s_waitcnt lgkmcnt(0)
	v_add_f32_e32 v48, v48, v49
	ds_bpermute_b32 v49, v80, v48
	s_waitcnt lgkmcnt(0)
	v_add_f32_e32 v48, v48, v49
	ds_bpermute_b32 v49, v81, v48
	s_waitcnt lgkmcnt(0)
	v_add_f32_e32 v50, v48, v49
	ds_bpermute_b32 v51, v82, v50
	v_lshl_add_u64 v[48:49], v[60:61], 0, s[4:5]
	s_lshl_b64 s[4:5], s[8:9], 2
	s_add_u32 s4, s20, s4
	s_addc_u32 s5, s21, s5
	s_waitcnt lgkmcnt(0)
	v_add_f32_e32 v50, v50, v51
	v_fmamk_f32 v50, v50, 0x3a800000, v85
	v_mul_f32_e32 v51, 0x4b800000, v50
	v_cmp_gt_f32_e32 vcc, s19, v50
	s_nop 1
	v_cndmask_b32_e32 v50, v50, v51, vcc
	v_rsq_f32_e32 v50, v50
	s_nop 0
	v_mul_f32_e32 v51, 0x45800000, v50
	v_cndmask_b32_e32 v50, v50, v51, vcc
	v_pk_mul_f32 v[0:1], v[0:1], v[50:51] op_sel_hi:[1,0]
	v_pk_mul_f32 v[2:3], v[2:3], v[50:51] op_sel_hi:[1,0]
	v_pk_mul_f32 v[4:5], v[4:5], v[50:51] op_sel_hi:[1,0]
	v_pk_mul_f32 v[6:7], v[6:7], v[50:51] op_sel_hi:[1,0]
	v_pk_mul_f32 v[8:9], v[8:9], v[50:51] op_sel_hi:[1,0]
	v_pk_mul_f32 v[10:11], v[10:11], v[50:51] op_sel_hi:[1,0]
	v_pk_mul_f32 v[64:65], v[14:15], v[50:51] op_sel_hi:[1,0]
	v_pk_mul_f32 v[12:13], v[12:13], v[50:51] op_sel_hi:[1,0]
	v_pk_mul_f32 v[2:3], v[26:27], v[2:3]
	v_pk_mul_f32 v[0:1], v[24:25], v[0:1]
	v_pk_mul_f32 v[6:7], v[30:31], v[6:7]
	v_pk_mul_f32 v[4:5], v[28:29], v[4:5]
	v_pk_mul_f32 v[10:11], v[42:43], v[10:11]
	v_pk_mul_f32 v[8:9], v[40:41], v[8:9]
	v_pk_mul_f32 v[14:15], v[46:47], v[12:13]
	v_pk_mul_f32 v[12:13], v[44:45], v[64:65]
	global_store_dwordx4 v[48:49], v[0:3], off
	global_store_dwordx4 v[48:49], v[4:7], off offset:1024
	global_store_dwordx4 v[48:49], v[8:11], off offset:2048
	global_store_dwordx4 v[48:49], v[12:15], off offset:3072
	v_readfirstlane_b32 s4, v204
	s_ashr_i32 s5, s4, 31
	s_lshl_b64 s[10:11], s[4:5], 2
	v_readfirstlane_b32 s8, v205
	s_add_u32 s10, s22, s10
	s_addc_u32 s11, s23, s11
	s_ashr_i32 s9, s8, 31
	s_lshl_b64 s[12:13], s[8:9], 2
	s_add_u32 s12, s22, s12
	s_addc_u32 s13, s23, s13
	s_ashr_i32 s0, s4, 14
	s_ashr_i32 s3, s8, 14
	s_lshl_b32 s0, s0, 2
	s_lshl_b32 s3, s3, 2
	s_add_i32 s0, s18, s0
	s_add_i32 s3, s18, s3
	v_mov_b32_e32 v2, s0
	v_mov_b32_e32 v3, s3
	ds_read_b32 v2, v2
	ds_read_b32 v3, v3
	s_and_b32 s0, s4, 0x3fff
	s_and_b32 s3, s8, 0x3fff
	s_mov_b64 s[12:13], -1
	s_waitcnt lgkmcnt(1)
	v_readfirstlane_b32 s4, v2
	s_waitcnt lgkmcnt(0)
	v_readfirstlane_b32 s5, v3
	s_lshl_b32 s4, s4, 8
	s_lshl_b32 s5, s5, 8
	s_add_i32 s10, s4, s0
	s_add_i32 s8, s5, s3
	s_max_i32 s0, s10, s8
	s_cmp_lt_i32 s0, 0x8000
	v_readfirstlane_b32 s4, v212
	v_readfirstlane_b32 s6, v213
	s_cbranch_scc1 .LBB0_1967
	v_mov_b32_e32 v48, 0
	v_mov_b32_e32 v49, v48
	v_mov_b32_e32 v50, v48
	v_mov_b32_e32 v51, v48
	v_mov_b32_e32 v0, v48
	v_mov_b32_e32 v1, v48
	v_mov_b32_e32 v64, v48
	v_mov_b32_e32 v65, v48
	v_mov_b32_e32 v66, v48
	v_mov_b32_e32 v67, v48
	v_mov_b32_e32 v68, v48
	v_mov_b32_e32 v69, v48
	v_mov_b32_e32 v70, v48
	v_mov_b32_e32 v71, v48
	v_mov_b32_e32 v72, v48
	v_mov_b32_e32 v73, v48
